# GB phase role placement: operand-staging role moved to hardware waves 2,3,6,7 so the two computing waves share their SIMDs with the idle waves instead of staging waves
# speedup vs baseline: 1.0067x; 1.0027x over previous
.LBB0_1627:
	v_mov_b32_e32 v1, v3
	s_lshr_b32 s1, s37, 3
	v_mov_b32_e32 v2, v0
	s_lshl_b32 s0, s37, 3
	s_and_b32 s1, s1, 6
	s_or_b32 s0, s1, s0
	v_readfirstlane_b32 s41, v2
	s_ashr_i32 s8, s41, 6
	s_and_b32 vcc_lo, s8, 4
	s_lshr_b32 vcc_lo, vcc_lo, 1
	s_xor_b32 s8, s8, vcc_lo
	s_bfe_u32 s39, s37, 0x10003
	s_bfe_u32 s3, s0, 0x30001
	s_bfe_u32 s38, s37, 0x20001
	s_and_b32 s2, s37, 0xffffffc0
	s_add_i32 s35, s8, -2
	v_and_b32_e32 v176, 63, v2
	s_cmp_gt_u32 s35, 3
	s_mov_b64 s[0:1], -1
	s_cbranch_scc1 .LBB0_1629
	s_andn2_b64 vcc, exec, s[0:1]
	s_cbranch_vccnz .LBB0_1626
	s_branch .LBB0_1639
